# baseline (speedup 1.0000x reference)
.LBB1_50:
	s_or_saveexec_b64 s[38:39], s[0:1]
	s_add_i32 s41, s67, s40
	s_mul_i32 s40, s69, 0x62
	s_xor_b64 exec, exec, s[38:39]
	s_cbranch_execz .LBB1_57
	v_mov_b32_e32 v35, 0
	ds_read_b32 v54, v35 offset:27144
	s_cmp_eq_u32 s68, 1
	s_cselect_b64 vcc, -1, 0
	v_sub_u32_e32 v46, v46, v31
	v_lshlrev_b32_e32 v55, 2, v0
	s_waitcnt lgkmcnt(0)
	v_cndmask_b32_e32 v56, 0, v54, vcc
	v_add_u32_e32 v46, v46, v56
	ds_write_b32 v55, v34 offset:27664
	v_add_u32_e32 v34, 0x6800, v55
	s_movk_i32 s0, 0x62
	ds_write2_b32 v34, v46, v31 offset1:132
	v_add_u32_e32 v34, s40, v0
	v_cmp_gt_u32_e32 vcc, s0, v0
	s_mov_b32 s0, 0x186a0
	v_cmp_gt_u32_e64 s[0:1], s0, v34
	s_and_b64 s[42:43], vcc, s[0:1]
	s_and_saveexec_b64 s[0:1], s[42:43]
	s_cbranch_execz .LBB1_53
	v_lshl_add_u64 v[34:35], v[34:35], 2, s[52:53]
	v_add_u32_e32 v31, s41, v46
	global_store_dword v[34:35], v31, off sc1
.LBB1_53:
	s_or_b64 exec, exec, s[0:1]
	v_cmp_eq_u32_e32 vcc, 0, v0
	s_and_saveexec_b64 s[0:1], vcc
	s_cbranch_execz .LBB1_56
	v_mov_b32_e32 v31, 0
	ds_read_b32 v34, v31 offset:27148
	s_cmpk_lg_i32 s69, 0x3fc
	s_waitcnt lgkmcnt(0)
	v_add_u32_e32 v34, v34, v54
	ds_write_b32 v31, v34 offset:27136
	s_cbranch_scc1 .LBB1_56
	v_mov_b32_e32 v31, 0x61000
	v_mov_b32_e32 v34, 0xf4240
	global_store_dword v31, v34, s[52:53] offset:2688 sc1

.LBB1_57:
	s_or_b64 exec, exec, s[38:39]
	s_waitcnt vmcnt(5)
	v_mov_b32_e32 v18, 0
	s_waitcnt lgkmcnt(0)
	s_barrier
	ds_read_b32 v46, v18 offset:27136
	s_movk_i32 s0, 0x801
	s_waitcnt lgkmcnt(0)
	v_cmp_gt_i32_e32 vcc, s0, v46
	s_mov_b64 s[0:1], -1
	s_cbranch_vccnz .LBB1_94
	s_and_saveexec_b64 s[0:1], s[30:31]
	s_cbranch_execz .LBB1_75
	s_waitcnt vmcnt(0)
	v_ashrrev_i32_e32 v18, 17, v14
	v_lshlrev_b32_e32 v18, 2, v18
	ds_read_b32 v18, v18 offset:26624
	v_and_b32_e32 v20, 0x1ffff, v14
	s_waitcnt lgkmcnt(0)
	v_add3_u32 v18, v18, s41, v53
	v_ashrrev_i32_e32 v19, 31, v18
	v_lshl_add_u64 v[18:19], v[18:19], 2, s[54:55]
	global_store_dword v[18:19], v20, off sc1
	s_or_b64 exec, exec, s[0:1]
	s_and_saveexec_b64 s[0:1], s[36:37]
	s_cbranch_execnz .LBB1_76

.LBB1_61:
	s_waitcnt vmcnt(0)
	v_ashrrev_i32_e32 v18, 17, v16
	v_lshlrev_b32_e32 v18, 2, v18
	ds_read_b32 v18, v18 offset:26624
	v_and_b32_e32 v20, 0x1ffff, v16
	s_waitcnt lgkmcnt(0)
	v_add3_u32 v18, v18, s41, v37
	v_ashrrev_i32_e32 v19, 31, v18
	v_lshl_add_u64 v[18:19], v[18:19], 2, s[54:55]
	global_store_dword v[18:19], v20, off sc1
	s_or_b64 exec, exec, s[0:1]
	s_and_saveexec_b64 s[0:1], s[4:5]
	s_cbranch_execnz .LBB1_78

.LBB1_63:
	s_waitcnt vmcnt(1)
	v_ashrrev_i32_e32 v18, 17, v10
	v_lshlrev_b32_e32 v18, 2, v18
	ds_read_b32 v18, v18 offset:26624
	v_and_b32_e32 v20, 0x1ffff, v10
	s_waitcnt lgkmcnt(0)
	v_add3_u32 v18, v18, s41, v39
	v_ashrrev_i32_e32 v19, 31, v18
	v_lshl_add_u64 v[18:19], v[18:19], 2, s[54:55]
	global_store_dword v[18:19], v20, off sc1
	s_or_b64 exec, exec, s[0:1]
	s_and_saveexec_b64 s[0:1], s[8:9]
	s_cbranch_execnz .LBB1_80

.LBB1_65:
	s_waitcnt vmcnt(1)
	v_ashrrev_i32_e32 v18, 17, v12
	v_lshlrev_b32_e32 v18, 2, v18
	ds_read_b32 v18, v18 offset:26624
	v_and_b32_e32 v20, 0x1ffff, v12
	s_waitcnt lgkmcnt(0)
	v_add3_u32 v18, v18, s41, v41
	v_ashrrev_i32_e32 v19, 31, v18
	v_lshl_add_u64 v[18:19], v[18:19], 2, s[54:55]
	global_store_dword v[18:19], v20, off sc1
	s_or_b64 exec, exec, s[0:1]
	s_and_saveexec_b64 s[0:1], s[12:13]
	s_cbranch_execnz .LBB1_82

.LBB1_67:
	s_waitcnt vmcnt(2)
	v_ashrrev_i32_e32 v18, 17, v6
	v_lshlrev_b32_e32 v18, 2, v18
	ds_read_b32 v18, v18 offset:26624
	v_and_b32_e32 v20, 0x1ffff, v6
	s_waitcnt lgkmcnt(0)
	v_add3_u32 v18, v18, s41, v43
	v_ashrrev_i32_e32 v19, 31, v18
	v_lshl_add_u64 v[18:19], v[18:19], 2, s[54:55]
	global_store_dword v[18:19], v20, off sc1
	s_or_b64 exec, exec, s[0:1]
	s_and_saveexec_b64 s[0:1], s[16:17]
	s_cbranch_execnz .LBB1_84

.LBB1_69:
	s_waitcnt vmcnt(2)
	v_ashrrev_i32_e32 v18, 17, v8
	v_lshlrev_b32_e32 v18, 2, v18
	ds_read_b32 v18, v18 offset:26624
	v_and_b32_e32 v20, 0x1ffff, v8
	s_waitcnt lgkmcnt(0)
	v_add3_u32 v18, v18, s41, v45
	v_ashrrev_i32_e32 v19, 31, v18
	v_lshl_add_u64 v[18:19], v[18:19], 2, s[54:55]
	global_store_dword v[18:19], v20, off sc1
	s_or_b64 exec, exec, s[0:1]
	s_and_saveexec_b64 s[0:1], s[20:21]
	s_cbranch_execnz .LBB1_86

.LBB1_71:
	s_waitcnt vmcnt(3)
	v_ashrrev_i32_e32 v18, 17, v2
	v_lshlrev_b32_e32 v18, 2, v18
	ds_read_b32 v18, v18 offset:26624
	v_and_b32_e32 v20, 0x1ffff, v2
	s_waitcnt lgkmcnt(0)
	v_add3_u32 v18, v18, s41, v49
	v_ashrrev_i32_e32 v19, 31, v18
	v_lshl_add_u64 v[18:19], v[18:19], 2, s[54:55]
	global_store_dword v[18:19], v20, off sc1
	s_or_b64 exec, exec, s[0:1]
	s_and_saveexec_b64 s[0:1], s[24:25]
	s_cbranch_execnz .LBB1_88

.LBB1_73:
	s_waitcnt vmcnt(3)
	v_ashrrev_i32_e32 v18, 17, v4
	v_lshlrev_b32_e32 v18, 2, v18
	ds_read_b32 v18, v18 offset:26624
	v_and_b32_e32 v20, 0x1ffff, v4
	s_waitcnt lgkmcnt(0)
	v_add3_u32 v18, v18, s41, v51
	v_ashrrev_i32_e32 v19, 31, v18
	v_lshl_add_u64 v[18:19], v[18:19], 2, s[54:55]
	global_store_dword v[18:19], v20, off sc1
	s_or_b64 exec, exec, s[0:1]
	s_and_saveexec_b64 s[0:1], s[28:29]
	s_cbranch_execnz .LBB1_90

.LBB1_76:
	s_waitcnt vmcnt(0)
	v_ashrrev_i32_e32 v18, 17, v15
	v_lshlrev_b32_e32 v18, 2, v18
	ds_read_b32 v18, v18 offset:26624
	v_and_b32_e32 v20, 0x1ffff, v15
	s_waitcnt lgkmcnt(0)
	v_add3_u32 v18, v18, s41, v36
	v_ashrrev_i32_e32 v19, 31, v18
	v_lshl_add_u64 v[18:19], v[18:19], 2, s[54:55]
	global_store_dword v[18:19], v20, off sc1
	s_or_b64 exec, exec, s[0:1]
	s_and_saveexec_b64 s[0:1], s[2:3]
	s_cbranch_execnz .LBB1_61

.LBB1_78:
	s_waitcnt vmcnt(0)
	v_ashrrev_i32_e32 v18, 17, v17
	v_lshlrev_b32_e32 v18, 2, v18
	ds_read_b32 v18, v18 offset:26624
	v_and_b32_e32 v20, 0x1ffff, v17
	s_waitcnt lgkmcnt(0)
	v_add3_u32 v18, v18, s41, v38
	v_ashrrev_i32_e32 v19, 31, v18
	v_lshl_add_u64 v[18:19], v[18:19], 2, s[54:55]
	global_store_dword v[18:19], v20, off sc1
	s_or_b64 exec, exec, s[0:1]
	s_and_saveexec_b64 s[0:1], s[6:7]
	s_cbranch_execnz .LBB1_63

.LBB1_80:
	s_waitcnt vmcnt(1)
	v_ashrrev_i32_e32 v18, 17, v11
	v_lshlrev_b32_e32 v18, 2, v18
	ds_read_b32 v18, v18 offset:26624
	v_and_b32_e32 v20, 0x1ffff, v11
	s_waitcnt lgkmcnt(0)
	v_add3_u32 v18, v18, s41, v40
	v_ashrrev_i32_e32 v19, 31, v18
	v_lshl_add_u64 v[18:19], v[18:19], 2, s[54:55]
	global_store_dword v[18:19], v20, off sc1
	s_or_b64 exec, exec, s[0:1]
	s_and_saveexec_b64 s[0:1], s[10:11]
	s_cbranch_execnz .LBB1_65

.LBB1_82:
	s_waitcnt vmcnt(1)
	v_ashrrev_i32_e32 v18, 17, v13
	v_lshlrev_b32_e32 v18, 2, v18
	ds_read_b32 v18, v18 offset:26624
	v_and_b32_e32 v20, 0x1ffff, v13
	s_waitcnt lgkmcnt(0)
	v_add3_u32 v18, v18, s41, v42
	v_ashrrev_i32_e32 v19, 31, v18
	v_lshl_add_u64 v[18:19], v[18:19], 2, s[54:55]
	global_store_dword v[18:19], v20, off sc1
	s_or_b64 exec, exec, s[0:1]
	s_and_saveexec_b64 s[0:1], s[14:15]
	s_cbranch_execnz .LBB1_67

.LBB1_84:
	s_waitcnt vmcnt(2)
	v_ashrrev_i32_e32 v18, 17, v7
	v_lshlrev_b32_e32 v18, 2, v18
	ds_read_b32 v18, v18 offset:26624
	v_and_b32_e32 v20, 0x1ffff, v7
	s_waitcnt lgkmcnt(0)
	v_add3_u32 v18, v18, s41, v44
	v_ashrrev_i32_e32 v19, 31, v18
	v_lshl_add_u64 v[18:19], v[18:19], 2, s[54:55]
	global_store_dword v[18:19], v20, off sc1
	s_or_b64 exec, exec, s[0:1]
	s_and_saveexec_b64 s[0:1], s[18:19]
	s_cbranch_execnz .LBB1_69

.LBB1_86:
	s_waitcnt vmcnt(2)
	v_ashrrev_i32_e32 v18, 17, v9
	v_lshlrev_b32_e32 v18, 2, v18
	ds_read_b32 v18, v18 offset:26624
	v_and_b32_e32 v20, 0x1ffff, v9
	s_waitcnt lgkmcnt(0)
	v_add3_u32 v18, v18, s41, v47
	v_ashrrev_i32_e32 v19, 31, v18
	v_lshl_add_u64 v[18:19], v[18:19], 2, s[54:55]
	global_store_dword v[18:19], v20, off sc1
	s_or_b64 exec, exec, s[0:1]
	s_and_saveexec_b64 s[0:1], s[22:23]
	s_cbranch_execnz .LBB1_71

.LBB1_88:
	s_waitcnt vmcnt(3)
	v_ashrrev_i32_e32 v18, 17, v3
	v_lshlrev_b32_e32 v18, 2, v18
	ds_read_b32 v18, v18 offset:26624
	v_and_b32_e32 v20, 0x1ffff, v3
	s_waitcnt lgkmcnt(0)
	v_add3_u32 v18, v18, s41, v50
	v_ashrrev_i32_e32 v19, 31, v18
	v_lshl_add_u64 v[18:19], v[18:19], 2, s[54:55]
	global_store_dword v[18:19], v20, off sc1
	s_or_b64 exec, exec, s[0:1]
	s_and_saveexec_b64 s[0:1], s[26:27]
	s_cbranch_execnz .LBB1_73

.LBB1_90:
	s_waitcnt vmcnt(3)
	v_ashrrev_i32_e32 v18, 17, v5
	v_lshlrev_b32_e32 v18, 2, v18
	ds_read_b32 v18, v18 offset:26624
	v_and_b32_e32 v20, 0x1ffff, v5
	s_waitcnt lgkmcnt(0)
	v_add3_u32 v18, v18, s41, v52
	v_ashrrev_i32_e32 v19, 31, v18
	v_lshl_add_u64 v[18:19], v[18:19], 2, s[54:55]
	global_store_dword v[18:19], v20, off sc1
	s_or_b64 exec, exec, s[0:1]
	s_and_saveexec_b64 s[0:1], s[34:35]
	s_cbranch_execz .LBB1_93

.LBB1_92:
	global_load_dword v22, v[18:19], off
	v_add_u32_e32 v21, 1, v21
	v_cmp_ge_i32_e32 vcc, v21, v33
	v_lshl_add_u64 v[18:19], v[18:19], 0, 4
	s_or_b64 s[38:39], vcc, s[38:39]
	s_waitcnt vmcnt(0)
	v_ashrrev_i32_e32 v23, 17, v22
	v_lshlrev_b32_e32 v23, 2, v23
	ds_add_rtn_u32 v24, v23, v20 offset:27664
	ds_read_b32 v23, v23 offset:26624
	v_and_b32_e32 v25, 0x1ffff, v22
	s_waitcnt lgkmcnt(0)
	v_add3_u32 v22, v24, s41, v23
	v_ashrrev_i32_e32 v23, 31, v22
	v_lshl_add_u64 v[22:23], v[22:23], 2, s[54:55]
	global_store_dword v[22:23], v25, off sc1
	s_andn2_b64 exec, exec, s[38:39]
	s_cbranch_execnz .LBB1_92

.LBB1_135:
	ds_read2st64_b32 v[4:5], v49 offset1:8
	v_add_u32_e32 v10, s41, v2
	ds_read2st64_b32 v[6:7], v49 offset0:16 offset1:24
	v_add_u32_e32 v47, -8, v47
	v_add_u32_e32 v8, s41, v3
	v_add_u32_e32 v16, s13, v2
	v_add_u32_e32 v14, s14, v3
	v_add_u32_e32 v22, s15, v2
	v_add_u32_e32 v20, s16, v3
	v_add_u32_e32 v28, s17, v2
	v_add_u32_e32 v26, s18, v3
	v_add_u32_e32 v34, s19, v2
	v_add_u32_e32 v32, s20, v3
	v_add_u32_e32 v40, s21, v2
	v_add_u32_e32 v38, s22, v3
	v_add_u32_e32 v52, s23, v2
	v_add_u32_e32 v54, s24, v3
	v_add_u32_e32 v56, s25, v2
	v_add_u32_e32 v58, s26, v3
	s_add_i32 s12, s12, 16
	v_ashrrev_i32_e32 v11, 31, v10
	v_cmp_eq_u32_e32 vcc, 0, v47
	ds_read2st64_b32 v[12:13], v49 offset0:32 offset1:40
	ds_read2st64_b32 v[18:19], v49 offset0:48 offset1:56
	ds_read2st64_b32 v[24:25], v49 offset0:64 offset1:72
	ds_read2st64_b32 v[30:31], v49 offset0:80 offset1:88
	ds_read2st64_b32 v[36:37], v49 offset0:96 offset1:104
	ds_read2st64_b32 v[42:43], v49 offset0:112 offset1:120
	v_add_u32_e32 v3, 0x2000, v3
	v_add_u32_e32 v2, 0x2000, v2
	v_add_u32_e32 v49, 0x8000, v49
	v_ashrrev_i32_e32 v9, 31, v8
	v_ashrrev_i32_e32 v15, 31, v14
	v_ashrrev_i32_e32 v17, 31, v16
	v_ashrrev_i32_e32 v21, 31, v20
	v_ashrrev_i32_e32 v23, 31, v22
	v_ashrrev_i32_e32 v27, 31, v26
	v_ashrrev_i32_e32 v29, 31, v28
	v_ashrrev_i32_e32 v33, 31, v32
	v_ashrrev_i32_e32 v35, 31, v34
	v_ashrrev_i32_e32 v39, 31, v38
	v_ashrrev_i32_e32 v41, 31, v40
	v_ashrrev_i32_e32 v55, 31, v54
	v_ashrrev_i32_e32 v53, 31, v52
	v_ashrrev_i32_e32 v59, 31, v58
	v_ashrrev_i32_e32 v57, 31, v56
	v_mov_b32_e32 v50, s12
	v_lshl_add_u64 v[10:11], v[10:11], 2, s[54:55]
	s_or_b64 s[10:11], vcc, s[10:11]
	v_lshl_add_u64 v[8:9], v[8:9], 2, s[54:55]
	v_lshl_add_u64 v[16:17], v[16:17], 2, s[54:55]
	v_lshl_add_u64 v[14:15], v[14:15], 2, s[54:55]
	v_lshl_add_u64 v[22:23], v[22:23], 2, s[54:55]
	v_lshl_add_u64 v[20:21], v[20:21], 2, s[54:55]
	v_lshl_add_u64 v[28:29], v[28:29], 2, s[54:55]
	v_lshl_add_u64 v[26:27], v[26:27], 2, s[54:55]
	v_lshl_add_u64 v[34:35], v[34:35], 2, s[54:55]
	v_lshl_add_u64 v[32:33], v[32:33], 2, s[54:55]
	v_lshl_add_u64 v[40:41], v[40:41], 2, s[54:55]
	v_lshl_add_u64 v[38:39], v[38:39], 2, s[54:55]
	v_lshl_add_u64 v[52:53], v[52:53], 2, s[54:55]
	v_lshl_add_u64 v[54:55], v[54:55], 2, s[54:55]
	v_lshl_add_u64 v[56:57], v[56:57], 2, s[54:55]
	v_lshl_add_u64 v[58:59], v[58:59], 2, s[54:55]
	s_waitcnt lgkmcnt(7)
	global_store_dword v[10:11], v4, off sc1
	global_store_dword v[8:9], v5, off sc1
	s_waitcnt lgkmcnt(6)
	global_store_dword v[16:17], v6, off sc1
	global_store_dword v[14:15], v7, off sc1
	s_waitcnt lgkmcnt(5)
	global_store_dword v[22:23], v12, off sc1
	global_store_dword v[20:21], v13, off sc1
	s_waitcnt lgkmcnt(4)
	global_store_dword v[28:29], v18, off sc1
	global_store_dword v[26:27], v19, off sc1
	s_waitcnt lgkmcnt(3)
	global_store_dword v[34:35], v24, off sc1
	global_store_dword v[32:33], v25, off sc1
	s_waitcnt lgkmcnt(2)
	global_store_dword v[40:41], v30, off sc1
	global_store_dword v[38:39], v31, off sc1
	s_waitcnt lgkmcnt(1)
	global_store_dword v[52:53], v36, off sc1
	global_store_dword v[54:55], v37, off sc1
	s_waitcnt lgkmcnt(0)
	global_store_dword v[56:57], v42, off sc1
	global_store_dword v[58:59], v43, off sc1
	s_andn2_b64 exec, exec, s[10:11]
	s_cbranch_execnz .LBB1_135
	s_or_b64 exec, exec, s[10:11]

.LBB1_139:
	ds_read2st64_b32 v[6:7], v4 offset1:8
	v_add_u32_e32 v8, s41, v2
	v_add_u32_e32 v1, -1, v1
	v_add_u32_e32 v10, s41, v3
	v_ashrrev_i32_e32 v9, 31, v8
	v_cmp_eq_u32_e32 vcc, 0, v1
	v_add_u32_e32 v3, 0x400, v3
	v_add_u32_e32 v2, 0x400, v2
	v_add_u32_e32 v4, 0x1000, v4
	v_ashrrev_i32_e32 v11, 31, v10
	v_lshl_add_u64 v[8:9], v[8:9], 2, s[54:55]
	s_or_b64 s[10:11], vcc, s[10:11]
	v_lshl_add_u64 v[10:11], v[10:11], 2, s[54:55]
	s_waitcnt lgkmcnt(0)
	global_store_dword v[8:9], v6, off sc1
	global_store_dword v[10:11], v7, off sc1
	s_andn2_b64 exec, exec, s[10:11]
	s_cbranch_execnz .LBB1_139

.LBB1_144:
	ds_read_b32 v5, v4
	v_add_u32_e32 v1, 0x200, v1
	v_ashrrev_i32_e32 v3, 31, v2
	v_cmp_ge_i32_e32 vcc, v1, v46
	v_add_u32_e32 v4, 0x800, v4
	v_lshl_add_u64 v[6:7], v[2:3], 2, s[54:55]
	v_add_u32_e32 v2, 0x200, v2
	s_or_b64 s[2:3], vcc, s[2:3]
	s_waitcnt lgkmcnt(0)
	global_store_dword v[6:7], v5, off sc1
	s_andn2_b64 exec, exec, s[2:3]
	s_cbranch_execnz .LBB1_144

.LBB1_158:
	s_or_b64 exec, exec, s[8:9]
	v_and_b32_e32 v9, 15, v0
	s_add_i32 s0, s16, s40
	v_cmp_gt_u32_e32 vcc, 14, v9
	v_add_u32_e32 v0, s0, v9
	s_and_b64 s[0:1], vcc, s[2:3]
	v_add_u32_e32 v1, s16, v9
	s_movk_i32 s2, 0x62
	v_cmp_gt_u32_e32 vcc, s2, v1
	s_mov_b32 s2, 0x186a0
	s_and_b64 s[0:1], s[0:1], vcc
	v_cmp_gt_u32_e32 vcc, s2, v0
	s_and_b64 s[0:1], s[0:1], vcc
	v_mov_b32_e32 v29, 0
	v_cndmask_b32_e64 v28, 0, v0, s[0:1]
	v_lshlrev_b64 v[0:1], 7, v[28:29]
	v_lshl_add_u64 v[0:1], s[56:57], 0, v[0:1]
	v_and_b32_e32 v20, -16, v48
	v_mov_b32_e32 v21, v29
	v_lshl_add_u64 v[0:1], v[0:1], 0, v[20:21]
	global_load_dwordx4 v[4:7], v[0:1], off
	s_nop 0
	global_load_dwordx4 v[0:3], v[0:1], off offset:64
	v_cvt_f32_i32_e32 v8, v51
	s_waitcnt vmcnt(3)
	v_lshrrev_b32_e32 v12, 4, v48
	v_lshlrev_b32_e32 v46, 4, v48
	v_max_f32_e32 v8, 1.0, v8
	v_div_scale_f32 v10, s[2:3], v8, v8, 1.0
	v_rcp_f32_e32 v11, v10
	s_nop 0
	v_fma_f32 v13, -v10, v11, 1.0
	v_fmac_f32_e32 v11, v13, v11
	v_div_scale_f32 v13, vcc, 1.0, v8, 1.0
	s_waitcnt vmcnt(2)
	v_mul_f32_e32 v14, v13, v11
	v_fma_f32 v15, -v10, v14, v13
	v_fmac_f32_e32 v14, v15, v11
	v_fma_f32 v10, -v10, v14, v13
	v_div_fmas_f32 v10, v10, v11, v14
	v_div_fixup_f32 v8, v10, v8, 1.0
	v_pk_mul_f32 v[10:11], v[8:9], v[44:45] op_sel_hi:[0,1]
	v_cvt_pk_f16_f32 v15, v10, v11
	v_pk_mul_f32 v[10:11], v[8:9], v[42:43] op_sel_hi:[0,1]
	v_cvt_pk_f16_f32 v16, v10, v11
	v_pk_mul_f32 v[10:11], v[8:9], v[40:41] op_sel_hi:[0,1]
	v_cvt_pk_f16_f32 v17, v10, v11
	v_pk_mul_f32 v[10:11], v[8:9], v[38:39] op_sel_hi:[0,1]
	v_cvt_pk_f16_f32 v18, v10, v11
	v_pk_mul_f32 v[10:11], v[8:9], v[36:37] op_sel_hi:[0,1]
	v_fma_mixlo_f16 v13, v8, v53, 0
	v_cvt_pk_f16_f32 v10, v10, v11
	v_pack_b32_f16 v13, v13, v15
	v_alignbit_b32 v15, v17, v15, 16
	v_alignbit_b32 v17, v10, v17, 16
	v_lshrrev_b32_e32 v19, 16, v10
	v_pk_mul_f32 v[10:11], v[8:9], v[34:35] op_sel_hi:[0,1]
	v_fma_mixlo_f16 v14, v8, v54, 0
	v_cvt_pk_f16_f32 v10, v10, v11
	v_pack_b32_f16 v14, v14, v16
	v_alignbit_b32 v16, v18, v16, 16
	v_alignbit_b32 v11, v10, v18, 16
	v_lshrrev_b32_e32 v18, 16, v10
	v_fma_mixhi_f16 v19, v8, v52, 0
	v_fma_mixhi_f16 v18, v8, v50, 0
	v_lshlrev_b32_e32 v8, 2, v9
	v_or3_b32 v8, v49, v8, v12
	v_lshlrev_b32_e32 v21, 2, v8
	ds_bpermute_b32 v12, v21, v13
	ds_bpermute_b32 v8, v21, v14
	ds_bpermute_b32 v13, v21, v15
	ds_bpermute_b32 v9, v21, v16
	ds_bpermute_b32 v14, v21, v17
	ds_bpermute_b32 v10, v21, v11
	ds_bpermute_b32 v15, v21, v19
	ds_bpermute_b32 v11, v21, v18
	global_load_dwordx4 v[16:19], v20, s[48:49]
	ds_read_b128 v[22:25], v46
	ds_read_b128 v[30:33], v46 offset:1024
	s_waitcnt vmcnt(0) lgkmcnt(1)
	v_mfma_f32_16x16x32_f16 v[16:19], v[22:25], v[12:15], v[16:19]
	ds_read_b128 v[22:25], v46 offset:2048
	s_waitcnt lgkmcnt(1)
	v_mfma_f32_16x16x32_f16 v[16:19], v[30:33], v[8:11], v[16:19]
	ds_read_b128 v[30:33], v46 offset:3072
	s_waitcnt lgkmcnt(1)
	v_mfma_f32_16x16x32_f16 v[16:19], v[22:25], v[4:7], v[16:19]
	s_waitcnt lgkmcnt(0)
	v_mfma_f32_16x16x32_f16 v[30:33], v[30:33], v[0:3], v[16:19]
	s_nop 5
	global_load_dwordx4 v[16:19], v20, s[48:49] offset:64
	ds_read_b128 v[22:25], v46 offset:4096
	ds_read_b128 v[34:37], v46 offset:5120
	s_waitcnt vmcnt(0) lgkmcnt(1)
	v_mfma_f32_16x16x32_f16 v[16:19], v[22:25], v[12:15], v[16:19]
	ds_read_b128 v[22:25], v46 offset:6144
	s_waitcnt lgkmcnt(1)
	v_mfma_f32_16x16x32_f16 v[16:19], v[34:37], v[8:11], v[16:19]
	ds_read_b128 v[34:37], v46 offset:7168
	s_waitcnt lgkmcnt(1)
	v_mfma_f32_16x16x32_f16 v[16:19], v[22:25], v[4:7], v[16:19]
	s_waitcnt lgkmcnt(0)
	v_mfma_f32_16x16x32_f16 v[34:37], v[34:37], v[0:3], v[16:19]
	s_nop 5
	global_load_dwordx4 v[16:19], v20, s[48:49] offset:128
	ds_read_b128 v[22:25], v46 offset:8192
	ds_read_b128 v[38:41], v46 offset:9216
	s_waitcnt vmcnt(0) lgkmcnt(1)
	v_mfma_f32_16x16x32_f16 v[16:19], v[22:25], v[12:15], v[16:19]
	ds_read_b128 v[22:25], v46 offset:10240
	s_waitcnt lgkmcnt(1)
	v_mfma_f32_16x16x32_f16 v[16:19], v[38:41], v[8:11], v[16:19]
	ds_read_b128 v[38:41], v46 offset:11264
	s_waitcnt lgkmcnt(1)
	v_mfma_f32_16x16x32_f16 v[16:19], v[22:25], v[4:7], v[16:19]
	s_waitcnt lgkmcnt(0)
	v_mfma_f32_16x16x32_f16 v[16:19], v[38:41], v[0:3], v[16:19]
	global_load_dwordx4 v[20:23], v20, s[48:49] offset:192
	ds_read_b128 v[24:27], v46 offset:12288
	s_load_dwordx2 s[2:3], s[50:51], 0x0
	v_max_f32_e32 v43, v34, v34
	v_max_f32_e32 v45, v35, v35
	v_max_f32_e32 v47, v36, v36
	v_max_f32_e32 v49, v37, v37
	ds_read_b128 v[34:37], v46 offset:24576
	ds_read_b128 v[38:41], v46 offset:25600
	v_max_f32_e32 v42, v30, v30
	v_max_f32_e32 v44, v31, v31
	v_max_f32_e32 v32, v32, v32
	v_max_f32_e32 v33, v33, v33
	v_max_f32_e32 v42, 0, v42
	v_max_f32_e32 v43, 0, v43
	v_max_f32_e32 v50, 0, v44
	v_max_f32_e32 v44, 0, v45
	v_max_f32_e32 v32, 0, v32
	v_max_f32_e32 v45, 0, v47
	v_max_f32_e32 v33, 0, v33
	v_max_f32_e32 v47, 0, v49
	v_mov_b32_e32 v30, v29
	v_mov_b32_e32 v31, v29
	v_cvt_pk_f16_f32 v45, v45, v47
	v_cvt_pk_f16_f32 v44, v43, v44
	v_cvt_pk_f16_f32 v43, v32, v33
	v_cvt_pk_f16_f32 v42, v42, v50
	s_waitcnt lgkmcnt(0)
	v_mov_b32_e32 v32, s2
	v_mov_b32_e32 v33, s3
	v_max_f32_e32 v16, v16, v16
	v_max_f32_e32 v17, v17, v17
	v_mfma_f32_16x16x32_f16 v[30:33], v[34:37], v[42:45], v[30:33]
	ds_read_b128 v[34:37], v46 offset:13312
	ds_read_b128 v[42:45], v46 offset:14336
	ds_read_b128 v[50:53], v46 offset:15360
	v_max_f32_e32 v18, v18, v18
	v_cmp_gt_u32_e32 vcc, 16, v48
	s_and_b64 s[0:1], s[0:1], vcc
	s_waitcnt vmcnt(0)
	v_mfma_f32_16x16x32_f16 v[12:15], v[24:27], v[12:15], v[20:23]
	s_waitcnt lgkmcnt(2)
	v_mfma_f32_16x16x32_f16 v[8:11], v[34:37], v[8:11], v[12:15]
	s_waitcnt lgkmcnt(1)
	v_mfma_f32_16x16x32_f16 v[4:7], v[42:45], v[4:7], v[8:11]
	s_nop 3
	v_max_f32_e32 v12, v19, v19
	v_max_f32_e32 v13, 0, v16
	v_max_f32_e32 v14, 0, v17
	s_waitcnt lgkmcnt(0)
	v_mfma_f32_16x16x32_f16 v[0:3], v[50:53], v[0:3], v[4:7]
	v_max_f32_e32 v8, 0, v18
	v_max_f32_e32 v9, 0, v12
	v_cvt_pk_f16_f32 v9, v8, v9
	v_cvt_pk_f16_f32 v8, v13, v14
	s_nop 3
	v_max_f32_e32 v0, v0, v0
	v_max_f32_e32 v1, v1, v1
	v_max_f32_e32 v2, v2, v2
	v_max_f32_e32 v3, v3, v3
	v_max_f32_e32 v0, 0, v0
	v_max_f32_e32 v1, 0, v1
	v_max_f32_e32 v2, 0, v2
	v_max_f32_e32 v3, 0, v3
	v_cvt_pk_f16_f32 v11, v2, v3
	v_cvt_pk_f16_f32 v10, v0, v1
	s_nop 1
	v_mfma_f32_16x16x32_f16 v[0:3], v[38:41], v[8:11], v[30:33]
	s_and_saveexec_b64 s[2:3], s[0:1]
	s_cbranch_execz .LBB1_160
	v_lshlrev_b64 v[4:5], 3, v[28:29]
	v_lshl_add_u64 v[6:7], s[44:45], 0, v[4:5]
	s_nop 3
	global_store_dwordx2 v[6:7], v[0:1], off sc1
	v_lshl_add_u64 v[0:1], s[46:47], 0, v[4:5]
	global_store_dwordx2 v[0:1], v[2:3], off sc1

.LBB2_22:
	s_or_b64 exec, exec, s[6:7]
	v_mov_b32_dpp v8, v6 quad_perm:[1,0,3,2] row_mask:0xf bank_mask:0xf bound_ctrl:1
	v_mov_b32_dpp v9, v7 quad_perm:[1,0,3,2] row_mask:0xf bank_mask:0xf bound_ctrl:1
	v_pk_add_f32 v[6:7], v[6:7], v[8:9]
	v_cmp_eq_u32_e64 s[0:1], 0, v0
	s_and_b64 s[0:1], s[0:1], vcc
	v_mov_b32_dpp v8, v6 quad_perm:[2,3,0,1] row_mask:0xf bank_mask:0xf bound_ctrl:1
	v_mov_b32_dpp v9, v7 quad_perm:[2,3,0,1] row_mask:0xf bank_mask:0xf bound_ctrl:1
	s_and_saveexec_b64 s[2:3], s[0:1]
	s_cbranch_execz .LBB2_24
	v_cvt_f32_i32_e32 v0, v24
	v_pk_add_f32 v[6:7], v[6:7], v[8:9]
	v_max_f32_e32 v10, 1.0, v0
	v_div_scale_f32 v11, s[0:1], v10, v10, 1.0
	s_waitcnt vmcnt(1)
	v_rcp_f32_e32 v12, v11
	s_waitcnt lgkmcnt(0)
	v_lshl_add_u64 v[0:1], v[2:3], 3, s[4:5]
	v_div_scale_f32 v2, vcc, 1.0, v10, 1.0
	v_fma_f32 v3, -v11, v12, 1.0
	v_fmac_f32_e32 v12, v3, v12
	v_mul_f32_e32 v3, v2, v12
	v_fma_f32 v13, -v11, v3, v2
	v_fmac_f32_e32 v3, v13, v12
	v_fma_f32 v2, -v11, v3, v2
	v_div_fmas_f32 v2, v2, v12, v3
	v_div_fixup_f32 v2, v2, v10, 1.0
	s_waitcnt vmcnt(0)
	v_pk_fma_f32 v[2:3], v[2:3], v[6:7], v[4:5] op_sel_hi:[0,1,1]
	global_store_dwordx2 v[0:1], v[2:3], off sc1
